# v123 + GLA pass-2 prologue: decay cut-off search loads issued together and waited once (was one dependent load + vmcnt(0) per earlier part), branch-free max scan
# baseline (speedup 1.0000x reference)
; #define GAS __attribute__((address_space(1)))
; #define LAS __attribute__((address_space(3)))
; template <bool NEEDQ>
; __device__ __forceinline__ void issue_loads(Stage& st, const bf16* QP, const bf16* KP, const bf16* VB, const float* BC, int tok0, int h, int s, int tid, unsigned qkoff, unsigned voff) {
;     const GAS char* qb = (const GAS char*)QP + (size_t)tok0 * KD * 2; const GAS char* kb = (const GAS char*)KP + (size_t)tok0 * KD * 2; const GAS char* vb = (const GAS char*)VB + (size_t)tok0 * VD * 2;
; #pragma unroll
;     for (int i = 0; i < 4; ++i) { if (NEEDQ) { st.q[i] = __builtin_nontemporal_load((const GAS v4u*)(qb + i * 16 * KD * 2 + qkoff)); st.k[i] = __builtin_nontemporal_load((const GAS v4u*)(kb + i * 16 * KD * 2 + qkoff)); } else st.k[i] = *(const GAS v4u*)(kb + i * 16 * KD * 2 + qkoff); }
; #pragma unroll
;     for (int i = 0; i < 2; ++i) st.v[i] = NEEDQ ? __builtin_nontemporal_load((const GAS v4u*)(vb + i * 32 * VD * 2 + voff)) : *(const GAS v4u*)(vb + i * 32 * VD * 2 + voff);
;     st.g = *(const GAS float*)((const GAS char*)BC + (size_t)(tok0 + 63) * KD * 4 + (unsigned)(h * DKH + (tid & 255)) * 4u);
; template <int PASS> ...
;     ...
;     f32x4 S[16];
; #pragma unroll
;     for (int dt = 0; dt < 16; ++dt) S[dt] = (f32x4){0.f, 0.f, 0.f, 0.f};
;     const int tokbase = p * CPP * CHK;
;     const unsigned qkoff = (unsigned)((tid >> 5) * KD + h * DKH + (tid & 31) * 8) * 2u, voff = (unsigned)((tid >> 4) * VD + h * DVH + s * 128 + (tid & 15) * 8) * 2u;
;     Stage st0, st1;
;     issue_loads<NQ>(st0, QP, KP, VB, BC, tokbase, h, s, tid, qkoff, voff);
;     __syncthreads();
;     if (PASS == 2 && p > 0) {
;         LAS int* cw = (LAS int*)(lds + OFF_P);
;         if (tid == 0) *cw = 1 << 30;
;         __syncthreads();
;         if (tid < 256) { float prod = 1.f; int j0 = 0; for (int j = p - 1; j >= 1; --j) { prod *= GTOT[((size_t)j * 4 + h) * DKH + tid]; if (prod < 1e-30f) { j0 = j; break; } }
;             __hip_atomic_fetch_min(cw, j0, __ATOMIC_RELAXED, __HIP_MEMORY_SCOPE_WORKGROUP); }
.LBB0_400:
	s_lshl_b32 s50, s91, 3
	s_and_b32 s50, s50, 56
	s_ashr_i32 s60, s91, 5
	s_add_i32 s50, s50, s60
	s_ashr_i32 s96, s50, 2
	s_and_b32 s95, s60, 3
	s_lshl_b32 s60, s96, 10
	s_bfe_u32 s92, s91, 0x20003
	s_ashr_i32 s61, s60, 31
	s_lshl_b32 s93, s95, 9
	s_lshl_b32 s94, s92, 7
	s_lshl_b64 s[62:63], s[60:61], 11
	v_or_b32_e32 v2, s93, v203
	s_add_u32 s66, s42, s62
	s_waitcnt lgkmcnt(0)
	v_or_b32_e32 v190, s93, v1
	v_or_b32_e32 v2, s94, v2
	s_addc_u32 s67, s43, s63
	v_lshlrev_b32_e32 v106, 1, v2
	s_add_u32 s62, s44, s62
	v_lshl_add_u64 v[2:3], s[66:67], 0, v[190:191]
	s_addc_u32 s63, s45, s63
	v_add_co_u32_e32 v6, vcc, s76, v2
	v_lshl_add_u64 v[4:5], s[62:63], 0, v[190:191]
	s_nop 0
	v_addc_co_u32_e32 v7, vcc, 0, v3, vcc
	v_add_co_u32_e32 v8, vcc, s76, v4
	s_lshl_b64 s[64:65], s[60:61], 12
	s_nop 0
	v_addc_co_u32_e32 v9, vcc, 0, v5, vcc
	global_load_dwordx4 v[42:45], v[6:7], off nt
	global_load_dwordx4 v[46:49], v[8:9], off nt
	v_add_co_u32_e32 v6, vcc, s77, v2
	s_add_u32 s68, s46, s64
	s_nop 0
	v_addc_co_u32_e32 v7, vcc, 0, v3, vcc
	v_add_co_u32_e32 v8, vcc, s77, v4
	s_addc_u32 s69, s47, s65
	s_nop 0
	v_addc_co_u32_e32 v9, vcc, 0, v5, vcc
	v_add_co_u32_e32 v2, vcc, s78, v2
	v_mov_b32_e32 v107, v191
	s_nop 0
	v_addc_co_u32_e32 v3, vcc, 0, v3, vcc
	v_add_co_u32_e32 v4, vcc, s78, v4
	global_load_dwordx4 v[50:53], v[6:7], off nt
	global_load_dwordx4 v[58:61], v[8:9], off nt
	v_addc_co_u32_e32 v5, vcc, 0, v5, vcc
	global_load_dwordx4 v[62:65], v[2:3], off nt
	global_load_dwordx4 v[66:69], v[4:5], off nt
	v_lshl_add_u64 v[2:3], s[68:69], 0, v[106:107]
	v_add_co_u32_e32 v2, vcc, s79, v2
	global_load_dwordx4 v[74:77], v106, s[68:69] nt
	s_nop 0
	v_addc_co_u32_e32 v3, vcc, 0, v3, vcc
	global_load_dwordx4 v[82:85], v190, s[66:67] nt
	global_load_dwordx4 v[78:81], v[2:3], off nt
	s_or_b32 s66, s60, 63
	s_ashr_i32 s67, s66, 31
	s_lshl_b64 s[66:67], s[66:67], 12
	s_add_u32 s66, s48, s66
	s_addc_u32 s67, s49, s67
	v_lshl_or_b32 v108, s95, 10, v218
	global_load_dwordx4 v[86:89], v190, s[62:63] nt
	global_load_dword v116, v108, s[66:67]
	s_cmp_lt_i32 s96, 1
	v_mov_b32_e32 v5, v191
	v_mov_b32_e32 v4, v191
	v_mov_b32_e32 v3, v191
	v_mov_b32_e32 v2, v191
	v_mov_b32_e32 v9, v191
	v_mov_b32_e32 v8, v191
	v_mov_b32_e32 v7, v191
	v_mov_b32_e32 v6, v191
	v_mov_b32_e32 v13, v191
	v_mov_b32_e32 v12, v191
	v_mov_b32_e32 v11, v191
	v_mov_b32_e32 v10, v191
	v_mov_b32_e32 v17, v191
	v_mov_b32_e32 v16, v191
	v_mov_b32_e32 v15, v191
	v_mov_b32_e32 v14, v191
	v_mov_b32_e32 v105, v191
	v_mov_b32_e32 v104, v191
	v_mov_b32_e32 v103, v191
	v_mov_b32_e32 v102, v191
	v_mov_b32_e32 v101, v191
	v_mov_b32_e32 v100, v191
	v_mov_b32_e32 v99, v191
	v_mov_b32_e32 v98, v191
	v_mov_b32_e32 v97, v191
	v_mov_b32_e32 v96, v191
	v_mov_b32_e32 v95, v191
	v_mov_b32_e32 v94, v191
	v_mov_b32_e32 v93, v191
	v_mov_b32_e32 v92, v191
	v_mov_b32_e32 v91, v191
	v_mov_b32_e32 v90, v191
	v_mov_b32_e32 v73, v191
	v_mov_b32_e32 v72, v191
	v_mov_b32_e32 v71, v191
	v_mov_b32_e32 v70, v191
	v_mov_b32_e32 v57, v191
	v_mov_b32_e32 v56, v191
	v_mov_b32_e32 v55, v191
	v_mov_b32_e32 v54, v191
	v_mov_b32_e32 v41, v191
	v_mov_b32_e32 v40, v191
	v_mov_b32_e32 v39, v191
	v_mov_b32_e32 v38, v191
	v_mov_b32_e32 v37, v191
	v_mov_b32_e32 v36, v191
	v_mov_b32_e32 v35, v191
	v_mov_b32_e32 v34, v191
	v_mov_b32_e32 v33, v191
	v_mov_b32_e32 v32, v191
	v_mov_b32_e32 v31, v191
	v_mov_b32_e32 v30, v191
	v_mov_b32_e32 v29, v191
	v_mov_b32_e32 v28, v191
	v_mov_b32_e32 v27, v191
	v_mov_b32_e32 v26, v191
	v_mov_b32_e32 v25, v191
	v_mov_b32_e32 v24, v191
	v_mov_b32_e32 v23, v191
	v_mov_b32_e32 v22, v191
	v_mov_b32_e32 v21, v191
	v_mov_b32_e32 v20, v191
	v_mov_b32_e32 v19, v191
	v_mov_b32_e32 v18, v191
	s_barrier
	s_cbranch_scc1 .LBB0_417
	s_and_saveexec_b64 s[62:63], s[4:5]
	v_mov_b32_e32 v2, s72
	v_mov_b32_e32 v3, 2.0
	ds_write_b32 v2, v3
	s_or_b64 exec, exec, s[62:63]
	s_waitcnt lgkmcnt(0)
	s_barrier
	s_and_saveexec_b64 s[62:63], s[6:7]
	s_cbranch_execz .LBB0_413
	s_add_i32 s50, s96, -1
	s_lshl_b64 s[66:67], s[50:51], 12
	s_lshl_b32 s50, s91, 5
	s_and_b32 s50, s50, 0xc00
	s_or_b32 s66, s66, s50
	v_lshl_add_u64 v[2:3], v[194:195], 0, s[66:67]
	v_mov_b32_e32 v4, 1.0
	v_mov_b32_e32 v5, 0
	s_mov_b32 s50, s96
	s_cmp_lt_i32 s50, 2
	s_cbranch_scc1 .Lmy_g2_issued
	global_load_dword v6, v[2:3], off
	v_lshl_add_u64 v[2:3], v[2:3], 0, s[52:53]
	s_cmp_lt_i32 s50, 3
	s_cbranch_scc1 .Lmy_g2_issued
	global_load_dword v7, v[2:3], off
	v_lshl_add_u64 v[2:3], v[2:3], 0, s[52:53]
	s_cmp_lt_i32 s50, 4
	s_cbranch_scc1 .Lmy_g2_issued
	global_load_dword v8, v[2:3], off
	v_lshl_add_u64 v[2:3], v[2:3], 0, s[52:53]
	s_cmp_lt_i32 s50, 5
	s_cbranch_scc1 .Lmy_g2_issued
	global_load_dword v9, v[2:3], off
	v_lshl_add_u64 v[2:3], v[2:3], 0, s[52:53]
	s_cmp_lt_i32 s50, 6
	s_cbranch_scc1 .Lmy_g2_issued
	global_load_dword v10, v[2:3], off
	v_lshl_add_u64 v[2:3], v[2:3], 0, s[52:53]
	s_cmp_lt_i32 s50, 7
	s_cbranch_scc1 .Lmy_g2_issued
	global_load_dword v11, v[2:3], off
	v_lshl_add_u64 v[2:3], v[2:3], 0, s[52:53]
	s_cmp_lt_i32 s50, 8
	s_cbranch_scc1 .Lmy_g2_issued
	global_load_dword v12, v[2:3], off
	v_lshl_add_u64 v[2:3], v[2:3], 0, s[52:53]
	s_cmp_lt_i32 s50, 9
	s_cbranch_scc1 .Lmy_g2_issued
	global_load_dword v13, v[2:3], off
	v_lshl_add_u64 v[2:3], v[2:3], 0, s[52:53]
	s_cmp_lt_i32 s50, 10
	s_cbranch_scc1 .Lmy_g2_issued
	global_load_dword v14, v[2:3], off
	v_lshl_add_u64 v[2:3], v[2:3], 0, s[52:53]
	s_cmp_lt_i32 s50, 11
	s_cbranch_scc1 .Lmy_g2_issued
	global_load_dword v15, v[2:3], off
	v_lshl_add_u64 v[2:3], v[2:3], 0, s[52:53]
	s_cmp_lt_i32 s50, 12
	s_cbranch_scc1 .Lmy_g2_issued
	global_load_dword v16, v[2:3], off
	v_lshl_add_u64 v[2:3], v[2:3], 0, s[52:53]
	s_cmp_lt_i32 s50, 13
	s_cbranch_scc1 .Lmy_g2_issued
	global_load_dword v17, v[2:3], off
	v_lshl_add_u64 v[2:3], v[2:3], 0, s[52:53]
	s_cmp_lt_i32 s50, 14
	s_cbranch_scc1 .Lmy_g2_issued
	global_load_dword v18, v[2:3], off
	v_lshl_add_u64 v[2:3], v[2:3], 0, s[52:53]
	s_cmp_lt_i32 s50, 15
	s_cbranch_scc1 .Lmy_g2_issued
	global_load_dword v19, v[2:3], off
	v_lshl_add_u64 v[2:3], v[2:3], 0, s[52:53]
; template <int PASS> ...
;     ...
;         if (tid < 256) { float prod = 1.f; int j0 = 0; for (int j = p - 1; j >= 1; --j) { prod *= GTOT[((size_t)j * 4 + h) * DKH + tid]; if (prod < 1e-30f) { j0 = j; break; } }
;             __hip_atomic_fetch_min(cw, j0, __ATOMIC_RELAXED, __HIP_MEMORY_SCOPE_WORKGROUP); }
.Lmy_g2_issued:
	s_waitcnt vmcnt(0)
	s_cmp_lt_i32 s50, 2
	s_cbranch_scc1 .Lmy_g2_done
	v_mul_f32_e32 v4, v4, v6
	v_cmp_gt_f32_e32 vcc, s80, v4
	s_sub_i32 s61, s50, 1
	v_mov_b32_e32 v21, s61
	s_nop 0
	v_cndmask_b32_e32 v20, 0, v21, vcc
	v_max_i32_e32 v5, v5, v20
	s_cmp_lt_i32 s50, 3
	s_cbranch_scc1 .Lmy_g2_done
	v_mul_f32_e32 v4, v4, v7
	v_cmp_gt_f32_e32 vcc, s80, v4
	s_sub_i32 s61, s50, 2
	v_mov_b32_e32 v21, s61
	s_nop 0
	v_cndmask_b32_e32 v20, 0, v21, vcc
	v_max_i32_e32 v5, v5, v20
	s_cmp_lt_i32 s50, 4
	s_cbranch_scc1 .Lmy_g2_done
	v_mul_f32_e32 v4, v4, v8
	v_cmp_gt_f32_e32 vcc, s80, v4
	s_sub_i32 s61, s50, 3
	v_mov_b32_e32 v21, s61
	s_nop 0
	v_cndmask_b32_e32 v20, 0, v21, vcc
	v_max_i32_e32 v5, v5, v20
	s_cmp_lt_i32 s50, 5
	s_cbranch_scc1 .Lmy_g2_done
	v_mul_f32_e32 v4, v4, v9
	v_cmp_gt_f32_e32 vcc, s80, v4
	s_sub_i32 s61, s50, 4
	v_mov_b32_e32 v21, s61
	s_nop 0
	v_cndmask_b32_e32 v20, 0, v21, vcc
	v_max_i32_e32 v5, v5, v20
	s_cmp_lt_i32 s50, 6
	s_cbranch_scc1 .Lmy_g2_done
	v_mul_f32_e32 v4, v4, v10
	v_cmp_gt_f32_e32 vcc, s80, v4
	s_sub_i32 s61, s50, 5
	v_mov_b32_e32 v21, s61
	s_nop 0
	v_cndmask_b32_e32 v20, 0, v21, vcc
	v_max_i32_e32 v5, v5, v20
	s_cmp_lt_i32 s50, 7
	s_cbranch_scc1 .Lmy_g2_done
	v_mul_f32_e32 v4, v4, v11
	v_cmp_gt_f32_e32 vcc, s80, v4
	s_sub_i32 s61, s50, 6
	v_mov_b32_e32 v21, s61
	s_nop 0
	v_cndmask_b32_e32 v20, 0, v21, vcc
	v_max_i32_e32 v5, v5, v20
	s_cmp_lt_i32 s50, 8
	s_cbranch_scc1 .Lmy_g2_done
	v_mul_f32_e32 v4, v4, v12
	v_cmp_gt_f32_e32 vcc, s80, v4
	s_sub_i32 s61, s50, 7
	v_mov_b32_e32 v21, s61
	s_nop 0
	v_cndmask_b32_e32 v20, 0, v21, vcc
	v_max_i32_e32 v5, v5, v20
	s_cmp_lt_i32 s50, 9
	s_cbranch_scc1 .Lmy_g2_done
	v_mul_f32_e32 v4, v4, v13
	v_cmp_gt_f32_e32 vcc, s80, v4
	s_sub_i32 s61, s50, 8
	v_mov_b32_e32 v21, s61
	s_nop 0
	v_cndmask_b32_e32 v20, 0, v21, vcc
	v_max_i32_e32 v5, v5, v20
	s_cmp_lt_i32 s50, 10
	s_cbranch_scc1 .Lmy_g2_done
	v_mul_f32_e32 v4, v4, v14
	v_cmp_gt_f32_e32 vcc, s80, v4
	s_sub_i32 s61, s50, 9
	v_mov_b32_e32 v21, s61
	s_nop 0
	v_cndmask_b32_e32 v20, 0, v21, vcc
	v_max_i32_e32 v5, v5, v20
	s_cmp_lt_i32 s50, 11
	s_cbranch_scc1 .Lmy_g2_done
	v_mul_f32_e32 v4, v4, v15
	v_cmp_gt_f32_e32 vcc, s80, v4
	s_sub_i32 s61, s50, 10
	v_mov_b32_e32 v21, s61
	s_nop 0
	v_cndmask_b32_e32 v20, 0, v21, vcc
	v_max_i32_e32 v5, v5, v20
	s_cmp_lt_i32 s50, 12
	s_cbranch_scc1 .Lmy_g2_done
	v_mul_f32_e32 v4, v4, v16
	v_cmp_gt_f32_e32 vcc, s80, v4
	s_sub_i32 s61, s50, 11
	v_mov_b32_e32 v21, s61
	s_nop 0
	v_cndmask_b32_e32 v20, 0, v21, vcc
	v_max_i32_e32 v5, v5, v20
	s_cmp_lt_i32 s50, 13
	s_cbranch_scc1 .Lmy_g2_done
	v_mul_f32_e32 v4, v4, v17
	v_cmp_gt_f32_e32 vcc, s80, v4
	s_sub_i32 s61, s50, 12
	v_mov_b32_e32 v21, s61
	s_nop 0
	v_cndmask_b32_e32 v20, 0, v21, vcc
	v_max_i32_e32 v5, v5, v20
	s_cmp_lt_i32 s50, 14
	s_cbranch_scc1 .Lmy_g2_done
	v_mul_f32_e32 v4, v4, v18
	v_cmp_gt_f32_e32 vcc, s80, v4
	s_sub_i32 s61, s50, 13
	v_mov_b32_e32 v21, s61
	s_nop 0
	v_cndmask_b32_e32 v20, 0, v21, vcc
	v_max_i32_e32 v5, v5, v20
	s_cmp_lt_i32 s50, 15
	s_cbranch_scc1 .Lmy_g2_done
	v_mul_f32_e32 v4, v4, v19
	v_cmp_gt_f32_e32 vcc, s80, v4
	s_sub_i32 s61, s50, 14
	v_mov_b32_e32 v21, s61
	s_nop 0
	v_cndmask_b32_e32 v20, 0, v21, vcc
	v_max_i32_e32 v5, v5, v20
.Lmy_g2_done:
	s_mov_b64 s[66:67], exec
	s_brev_b32 s50, -2
